# NSA phase: the 16 workgroups of a (batch, kv group) mapped to one XCD (shared K/V tiles hit L2)
# baseline (speedup 1.0000x reference)
.LBB0_891:
	s_or_b64 exec, exec, s[0:1]
	s_waitcnt vmcnt(7)
	v_cndmask_b32_e64 v2, 0, 1, s[4:5]
	v_cmp_ne_u32_e64 s[0:1], 1, v2
	s_waitcnt lgkmcnt(0)
	v_mov_b32_e32 v1, v0
	s_andn2_b64 vcc, exec, s[4:5]
	v_writelane_b32 v251, s0, 8
	s_barrier
	s_nop 0
	v_writelane_b32 v251, s1, 9
	s_cbranch_vccnz .LBB0_931
	v_writelane_b32 v251, s89, 10
	v_writelane_b32 v251, s94, 11
	v_writelane_b32 v252, s92, 62
	s_mov_b32 s97, 0
	v_writelane_b32 v251, s95, 12
	v_writelane_b32 v252, s93, 63
	v_writelane_b32 v251, s90, 13
	v_readlane_b32 s0, v252, 0
	v_readlane_b32 s1, v252, 6
	v_writelane_b32 v251, s91, 14
	s_lshr_b32 s4, s0, 7
	s_lshl_b32 s0, s1, 5
	v_writelane_b32 v251, s88, 15
	s_and_b32 s0, s0, 32
	v_writelane_b32 v252, s0, 58
	v_writelane_b32 v251, s89, 16
	s_add_u32 s0, s84, 0x15000000
	v_writelane_b32 v251, s0, 17
	s_addc_u32 s0, s85, 0
	v_writelane_b32 v251, s0, 18
	s_mul_i32 s0, s1, 0x1200
	s_add_u32 s1, s84, 0x8000000
	v_writelane_b32 v251, s1, 19
	s_addc_u32 s1, s85, 0
	v_writelane_b32 v251, s1, 20
	s_add_u32 s1, s84, 0x1d400000
	v_writelane_b32 v251, s1, 21
	s_addc_u32 s1, s85, 0
	v_writelane_b32 v251, s1, 22
	s_add_i32 s92, s0, 0
	v_writelane_b32 v251, s4, 23
	s_lshl_b32 s0, s4, 11
	s_mov_b64 s[4:5], s[80:81]
	v_writelane_b32 v251, s0, 24
	s_mov_b64 s[6:7], s[82:83]
	s_mov_b64 s[8:9], s[84:85]
	v_writelane_b32 v251, s4, 25
	s_add_u32 s0, s84, 0x100000
	s_addc_u32 s1, s85, 0
	v_writelane_b32 v251, s5, 26
	v_writelane_b32 v251, s6, 27
	v_writelane_b32 v251, s7, 28
	v_writelane_b32 v251, s8, 29
	v_writelane_b32 v251, s9, 30
	v_writelane_b32 v251, s10, 31
	v_writelane_b32 v251, s11, 32
	v_writelane_b32 v251, s0, 33
	v_mov_b32_e32 v2, 0
	s_movk_i32 s82, 0x4000
	v_writelane_b32 v251, s1, 34
	s_mov_b32 s0, s96
	v_writelane_b32 v251, s0, 35
	v_mov_b32_e32 v194, 0xff800000
	s_mov_b32 s83, 0x41380000
	v_mov_b32_e32 v195, 0xf149f2ca
	s_add_i32 s85, 0, 0x12800
	v_mov_b32_e32 v196, 0x447a0000
	v_mov_b32_e32 v197, 0xc47a0000
	v_mbcnt_hi_u32_b32 v198, -1, v228
	v_writelane_b32 v251, s1, 36
	s_mov_b32 s1, s96
	v_readlane_b32 s100, v252, 41
	s_nop 3
	s_cmpk_lg_i32 s100, 0x100
	s_cbranch_scc1 .Lmy_nsa_nomap
	s_and_b32 s1, s96, 7
	s_lshl_b32 s1, s1, 1
	s_bfe_u32 s100, s96, 0x10003
	s_add_i32 s1, s1, s100
	s_lshl_b32 s1, s1, 4
	s_lshr_b32 s100, s96, 4
	s_add_i32 s1, s1, s100
.Lmy_nsa_nomap:
	s_branch .LBB0_894
.LBB0_893:
	v_readlane_b32 s43, v252, 41
	v_readlane_b32 s1, v251, 37
	s_add_i32 s1, s1, s43
	s_cmpk_gt_i32 s1, 0xff
	s_cbranch_scc1 .LBB0_930
